# GQA-latent attention tile loop rewritten by hand (fewer instrs: no S copies, simplified tile addressing, QK MFMAs interleaved with row-max chain)
# speedup vs baseline: 1.0831x; 1.0090x over previous
.LBB0_703:
	s_andn2_b64 vcc, exec, s[0:1]
	s_cbranch_vccnz .LBB0_907
	s_add_i32 s0, s35, 7
	v_add_u32_e32 v0, s2, v4
	s_and_b32 s12, s0, -4
	v_med3_u32 v1, v0, 8, 56
	s_bfe_u32 s0, s33, 0x60019
	s_add_i32 s0, s33, s0
	v_sub_u32_e32 v1, v209, v1
	s_sext_i32_i16 s0, s0
	v_add_u32_e32 v2, 8, v1
	s_ashr_i32 s10, s0, 6
	v_cmp_gt_u32_e64 s[0:1], 16, v2
	v_mad_u32_u24 v210, v4, s58, 0
	v_lshlrev_b32_e32 v3, 3, v4
	v_writelane_b32 v255, s0, 6
	v_sub_u32_e32 v211, v210, v3
	v_and_b32_e32 v3, -16, v2
	v_writelane_b32 v255, s1, 7
	s_movk_i32 s0, 0xffe0
	v_cmp_eq_u32_e64 s[42:43], s0, v3
	v_add_u32_e32 v4, 9, v1
	s_movk_i32 s0, 0xffef
	v_cmp_gt_u32_e64 s[44:45], 16, v4
	v_add_u32_e32 v4, 41, v1
	v_cmp_lt_u32_e64 s[72:73], s0, v2
	v_add_u32_e32 v2, 25, v1
	v_cmp_gt_u32_e64 s[46:47], 16, v4
	v_add_u32_e32 v4, 10, v1
	v_cmp_gt_u32_e64 s[76:77], 16, v2
	v_add_u32_e32 v2, 57, v1
	v_cmp_gt_u32_e64 s[48:49], 16, v4
	v_add_u32_e32 v4, 42, v1
	v_cmp_gt_u32_e64 s[78:79], 16, v2
	v_add_u32_e32 v2, 26, v1
	v_cmp_gt_u32_e64 s[50:51], 16, v4
	v_add_u32_e32 v4, 11, v1
	v_cmp_gt_u32_e64 s[80:81], 16, v2
	v_add_u32_e32 v2, 58, v1
	v_cmp_gt_u32_e64 s[52:53], 16, v4
	v_add_u32_e32 v4, 43, v1
	v_cmp_gt_u32_e64 s[82:83], 16, v2
	v_add_u32_e32 v2, 27, v1
	v_cmp_gt_u32_e64 s[54:55], 16, v4
	v_add_u32_e32 v4, 16, v1
	v_cmp_gt_u32_e64 s[84:85], 16, v2
	v_add_u32_e32 v2, 59, v1
	v_cmp_gt_u32_e64 s[56:57], 16, v4
	v_add_u32_e32 v4, 48, v1
	v_cmp_gt_u32_e64 s[86:87], 16, v2
	v_add_u32_e32 v2, 32, v1
	v_cmp_gt_u32_e64 s[58:59], 16, v4
	v_add_u32_e32 v4, 17, v1
	v_cmp_gt_u32_e64 s[88:89], 16, v2
	v_add_u32_e32 v2, 64, v1
	v_cmp_gt_u32_e64 s[60:61], 16, v4
	v_add_u32_e32 v4, 49, v1
	v_cmp_gt_u32_e64 s[90:91], 16, v2
	v_add_u32_e32 v2, 33, v1
	v_cmp_gt_u32_e64 s[62:63], 16, v4
	v_add_u32_e32 v4, 18, v1
	v_cmp_gt_u32_e64 s[92:93], 16, v2
	v_add_u32_e32 v2, 0x41, v1
	v_cmp_gt_u32_e64 s[64:65], 16, v4
	v_add_u32_e32 v4, 50, v1
	v_cmp_gt_u32_e64 s[94:95], 16, v2
	v_add_u32_e32 v2, 34, v1
	v_cmp_gt_u32_e64 s[66:67], 16, v4
	v_add_u32_e32 v4, 19, v1
	v_cmp_gt_u32_e64 s[96:97], 16, v2
	v_add_u32_e32 v2, 0x42, v1
	s_mulk_i32 s10, 0x7c
	v_lshlrev_b32_e32 v0, 2, v0
	v_cmp_gt_u32_e64 s[68:69], 16, v4
	v_add_u32_e32 v4, 51, v1
	s_movk_i32 s0, 0xffd0
	v_cmp_gt_u32_e64 s[4:5], 16, v2
	v_add_u32_e32 v2, 35, v1
	v_add_u32_e32 v1, 0x43, v1
	v_sub_u32_e32 v0, s10, v0
	s_mul_i32 s10, s14, 0x7c
	v_mov_b32_e32 v32, v193
	v_mov_b32_e32 v33, v193
	v_cmp_gt_u32_e64 s[70:71], 16, v4
	v_cmp_eq_u32_e64 s[74:75], s0, v3
	v_cmp_gt_u32_e64 s[6:7], 16, v2
	v_cmp_gt_u32_e64 s[8:9], 16, v1
	v_subrev_u32_e32 v213, s10, v0
	v_readlane_b32 s10, v254, 25
	v_mov_b32_e32 v34, v193
	v_mov_b32_e32 v35, v193
	v_mov_b32_e32 v36, v193
	v_mov_b32_e32 v37, v193
	v_mov_b32_e32 v38, v193
	v_mov_b32_e32 v39, v193
	v_mov_b32_e32 v40, v193
	v_mov_b32_e32 v41, v193
	v_mov_b32_e32 v42, v193
	v_mov_b32_e32 v43, v193
	v_mov_b32_e32 v44, v193
	v_mov_b32_e32 v45, v193
	v_mov_b32_e32 v46, v193
	v_mov_b32_e32 v47, v193
	v_mov_b64_e32 v[0:1], v[32:33]
	v_mov_b64_e32 v[16:17], v[32:33]
	s_add_i32 s28, s35, 4
	s_add_i32 s2, s21, 7
	s_mov_b64 s[16:17], -1
	s_xor_b64 s[0:1], s[36:37], -1
	v_add_u32_e32 v214, s10, v208
	s_mov_b32 s29, 0
	v_mov_b32_e32 v212, 0
	v_mov_b32_e32 v215, 0
	v_mov_b64_e32 v[2:3], v[34:35]
	v_mov_b64_e32 v[4:5], v[36:37]
	v_mov_b64_e32 v[6:7], v[38:39]
	v_mov_b64_e32 v[8:9], v[40:41]
	v_mov_b64_e32 v[10:11], v[42:43]
	v_mov_b64_e32 v[12:13], v[44:45]
	v_mov_b64_e32 v[14:15], v[46:47]
	v_mov_b64_e32 v[18:19], v[34:35]
	v_mov_b64_e32 v[20:21], v[36:37]
	v_mov_b64_e32 v[22:23], v[38:39]
	v_mov_b64_e32 v[24:25], v[40:41]
	v_mov_b64_e32 v[26:27], v[42:43]
	v_mov_b64_e32 v[28:29], v[44:45]
	v_mov_b64_e32 v[30:31], v[46:47]
	s_cmp_eq_u32 s35, 64
	s_cbranch_scc1 .Lfa_entry

.Lfa_entry:
	s_mov_b32 s29, 0
	s_mov_b32 s40, 1
	s_add_i32 s41, s23, 0xfffff000
	s_movk_i32 s10, 0x6a00
	v_add3_u32 v217, v201, v202, s10
.Lfa_loop:
	s_add_i32 s10, s29, 6
	s_min_i32 s10, s10, 0x43
	s_cmp_lt_i32 s10, 64
	s_cselect_b32 s11, s20, s41
	s_lshl_b32 s10, s10, 6
	s_add_i32 s10, s10, s11
	v_add_u32_e32 v112, s10, v197
	s_movk_i32 s10, 0x4a00
	v_mad_i64_i32 v[112:113], s[10:11], v112, s10, v[204:205]
	s_add_i32 s14, s29, 5
	s_min_i32 s14, s14, 0x43
	s_lshl_b32 s14, s14, 6
	s_mov_b32 s15, 0
	s_waitcnt vmcnt(7)
	ds_write_b128 v199, v[164:167]
	s_waitcnt vmcnt(6)
	ds_write2_b64 v217, v[160:161], v[162:163] offset1:1
	v_lshl_add_u64 v[114:115], s[14:15], 1, v[206:207]
	v_add_u32_e32 v216, v210, v208
	global_load_dwordx4 v[164:167], v[112:113], off
	global_load_dwordx4 v[160:163], v[114:115], off
	ds_read_b128 v[112:115], v216 offset:17920
	ds_read_b128 v[116:119], v216 offset:22528
	ds_read_b128 v[120:123], v216 offset:17952
	ds_read_b128 v[124:127], v216 offset:22560
	ds_read_b128 v[128:131], v216 offset:17984
	ds_read_b128 v[132:135], v216 offset:22592
	ds_read_b128 v[136:139], v216 offset:18016
	ds_read_b128 v[140:143], v216 offset:22624
	s_waitcnt lgkmcnt(7)
	v_mfma_f32_32x32x16_bf16 v[80:95], v[112:115], v[144:147], v[32:47]
	v_max3_f32 v214, v48, v64, v49
	v_max3_f32 v214, v214, v65, v50
	s_waitcnt lgkmcnt(6)
	v_mfma_f32_32x32x16_bf16 v[96:111], v[116:119], v[144:147], v[32:47]
	v_max3_f32 v214, v214, v66, v51
	v_max3_f32 v214, v214, v67, v52
	s_waitcnt lgkmcnt(5)
	v_mfma_f32_32x32x16_bf16 v[80:95], v[120:123], v[148:151], v[80:95]
	v_max3_f32 v214, v214, v68, v53
	v_max3_f32 v214, v214, v69, v54
	s_waitcnt lgkmcnt(4)
	v_mfma_f32_32x32x16_bf16 v[96:111], v[124:127], v[148:151], v[96:111]
	v_max3_f32 v214, v214, v70, v55
	v_max3_f32 v214, v214, v71, v56
	s_waitcnt lgkmcnt(3)
	v_mfma_f32_32x32x16_bf16 v[80:95], v[128:131], v[152:155], v[80:95]
	v_max3_f32 v214, v214, v72, v57
	v_max3_f32 v214, v214, v73, v58
	s_waitcnt lgkmcnt(2)
	v_mfma_f32_32x32x16_bf16 v[96:111], v[132:135], v[152:155], v[96:111]
	v_max3_f32 v214, v214, v74, v59
	v_max3_f32 v214, v214, v75, v60
	s_waitcnt lgkmcnt(1)
	v_mfma_f32_32x32x16_bf16 v[80:95], v[136:139], v[156:159], v[80:95]
	v_max3_f32 v214, v214, v76, v61
	v_max3_f32 v214, v214, v77, v62
	s_waitcnt lgkmcnt(0)
	v_mfma_f32_32x32x16_bf16 v[96:111], v[140:143], v[156:159], v[96:111]
	v_max3_f32 v214, v214, v78, v63
	v_max_f32_e32 v214, v214, v79
	ds_bpermute_b32 v218, v227, v214
	v_add_u32_e32 v140, v211, v200
	v_add_u32_e32 v141, 13568, v140
	v_add_u32_e32 v140, 9216, v140
	ds_read2_b64 v[112:115], v140 offset1:2
	ds_read2_b64 v[116:119], v141 offset1:2
	ds_read2_b64 v[120:123], v140 offset0:4 offset1:6
	ds_read2_b64 v[124:127], v141 offset0:4 offset1:6
	ds_read2_b64 v[128:131], v140 offset0:8 offset1:10
	ds_read2_b64 v[132:135], v141 offset0:8 offset1:10
	ds_read2_b64 v[136:139], v140 offset0:12 offset1:14
	ds_read2_b64 v[140:143], v141 offset0:12 offset1:14
	s_waitcnt lgkmcnt(8)
	v_max_f32_e32 v214, v214, v218
	s_cmp_lg_u32 s40, 0
	s_cbranch_scc1 .Lfa_resc0
	v_cmp_lt_f32_e32 vcc, 0x40c00000, v214
	s_cbranch_vccnz .Lfa_resc0
.Lfa_cont0:
	v_exp_f32_e32 v48, v48
	v_exp_f32_e32 v49, v49
	v_exp_f32_e32 v50, v50
	v_exp_f32_e32 v51, v51
	v_exp_f32_e32 v52, v52
	v_exp_f32_e32 v53, v53
	v_exp_f32_e32 v54, v54
	v_exp_f32_e32 v55, v55
	v_add_f32_e32 v216, v48, v49
	v_add_f32_e32 v216, v216, v50
	v_add_f32_e32 v216, v216, v51
	v_add_f32_e32 v216, v216, v52
	v_add_f32_e32 v216, v216, v53
	v_add_f32_e32 v216, v216, v54
	v_add_f32_e32 v216, v216, v55
	v_cvt_pk_bf16_f32 v48, v48, v49
	v_cvt_pk_bf16_f32 v49, v50, v51
	v_cvt_pk_bf16_f32 v50, v52, v53
	v_cvt_pk_bf16_f32 v51, v54, v55
	v_exp_f32_e32 v56, v56
	v_exp_f32_e32 v57, v57
	v_exp_f32_e32 v58, v58
	v_exp_f32_e32 v59, v59
	s_waitcnt lgkmcnt(7)
	v_mfma_f32_32x32x16_bf16 v[0:15], v[112:115], v[48:51], v[0:15]
	v_exp_f32_e32 v60, v60
	v_exp_f32_e32 v61, v61
	v_exp_f32_e32 v62, v62
	v_exp_f32_e32 v63, v63
	s_waitcnt lgkmcnt(6)
	v_mfma_f32_32x32x16_bf16 v[16:31], v[116:119], v[48:51], v[16:31]
	v_add_f32_e32 v216, v216, v56
	v_add_f32_e32 v216, v216, v57
	v_add_f32_e32 v216, v216, v58
	v_add_f32_e32 v216, v216, v59
	v_add_f32_e32 v216, v216, v60
	v_add_f32_e32 v216, v216, v61
	v_add_f32_e32 v216, v216, v62
	v_add_f32_e32 v216, v216, v63
	v_cvt_pk_bf16_f32 v56, v56, v57
	v_cvt_pk_bf16_f32 v57, v58, v59
	v_cvt_pk_bf16_f32 v58, v60, v61
	v_cvt_pk_bf16_f32 v59, v62, v63
	v_exp_f32_e32 v64, v64
	v_exp_f32_e32 v65, v65
	v_exp_f32_e32 v66, v66
	v_exp_f32_e32 v67, v67
	s_waitcnt lgkmcnt(5)
	v_mfma_f32_32x32x16_bf16 v[0:15], v[120:123], v[56:59], v[0:15]
	v_exp_f32_e32 v68, v68
	v_exp_f32_e32 v69, v69
	v_exp_f32_e32 v70, v70
	v_exp_f32_e32 v71, v71
	s_waitcnt lgkmcnt(4)
	v_mfma_f32_32x32x16_bf16 v[16:31], v[124:127], v[56:59], v[16:31]
	v_add_f32_e32 v216, v216, v64
	v_add_f32_e32 v216, v216, v65
	v_add_f32_e32 v216, v216, v66
	v_add_f32_e32 v216, v216, v67
	v_add_f32_e32 v216, v216, v68
	v_add_f32_e32 v216, v216, v69
	v_add_f32_e32 v216, v216, v70
	v_add_f32_e32 v216, v216, v71
	v_cvt_pk_bf16_f32 v64, v64, v65
	v_cvt_pk_bf16_f32 v65, v66, v67
	v_cvt_pk_bf16_f32 v66, v68, v69
	v_cvt_pk_bf16_f32 v67, v70, v71
	v_exp_f32_e32 v72, v72
	v_exp_f32_e32 v73, v73
	v_exp_f32_e32 v74, v74
	v_exp_f32_e32 v75, v75
	s_waitcnt lgkmcnt(3)
	v_mfma_f32_32x32x16_bf16 v[0:15], v[128:131], v[64:67], v[0:15]
	v_exp_f32_e32 v76, v76
	v_exp_f32_e32 v77, v77
	v_exp_f32_e32 v78, v78
	v_exp_f32_e32 v79, v79
	s_waitcnt lgkmcnt(2)
	v_mfma_f32_32x32x16_bf16 v[16:31], v[132:135], v[64:67], v[16:31]
	v_add_f32_e32 v216, v216, v72
	v_add_f32_e32 v216, v216, v73
	v_add_f32_e32 v216, v216, v74
	v_add_f32_e32 v216, v216, v75
	v_add_f32_e32 v216, v216, v76
	v_add_f32_e32 v216, v216, v77
	v_add_f32_e32 v216, v216, v78
	v_add_f32_e32 v216, v216, v79
	v_cvt_pk_bf16_f32 v72, v72, v73
	v_cvt_pk_bf16_f32 v73, v74, v75
	v_cvt_pk_bf16_f32 v74, v76, v77
	v_cvt_pk_bf16_f32 v75, v78, v79
	v_add_f32_e32 v212, v212, v216
	s_waitcnt lgkmcnt(1)
	v_mfma_f32_32x32x16_bf16 v[0:15], v[136:139], v[72:75], v[0:15]
	s_waitcnt lgkmcnt(0)
	v_mfma_f32_32x32x16_bf16 v[16:31], v[140:143], v[72:75], v[16:31]
	s_barrier
	s_add_i32 s10, s29, 7
	s_min_i32 s10, s10, 0x43
	s_cmp_lt_i32 s10, 64
	s_cselect_b32 s11, s20, s41
	s_lshl_b32 s10, s10, 6
	s_add_i32 s10, s10, s11
	v_add_u32_e32 v112, s10, v197
	s_movk_i32 s10, 0x4a00
	v_mad_i64_i32 v[112:113], s[10:11], v112, s10, v[204:205]
	s_add_i32 s14, s29, 6
	s_min_i32 s14, s14, 0x43
	s_lshl_b32 s14, s14, 6
	s_mov_b32 s15, 0
	s_waitcnt vmcnt(7)
	ds_write_b128 v199, v[168:171] offset:17920
	s_waitcnt vmcnt(6)
	ds_write2_b64 v203, v[172:173], v[174:175] offset1:1
	v_lshl_add_u64 v[114:115], s[14:15], 1, v[206:207]
	v_add_u32_e32 v216, v210, v208
	global_load_dwordx4 v[168:171], v[112:113], off
	global_load_dwordx4 v[172:175], v[114:115], off
	ds_read_b128 v[112:115], v216
	ds_read_b128 v[116:119], v216 offset:4608
	ds_read_b128 v[120:123], v216 offset:32
	ds_read_b128 v[124:127], v216 offset:4640
	ds_read_b128 v[128:131], v216 offset:64
	ds_read_b128 v[132:135], v216 offset:4672
	ds_read_b128 v[136:139], v216 offset:96
	ds_read_b128 v[140:143], v216 offset:4704
	s_waitcnt lgkmcnt(7)
	v_mfma_f32_32x32x16_bf16 v[48:63], v[112:115], v[144:147], v[32:47]
	v_max3_f32 v214, v80, v96, v81
	v_max3_f32 v214, v214, v97, v82
	s_waitcnt lgkmcnt(6)
	v_mfma_f32_32x32x16_bf16 v[64:79], v[116:119], v[144:147], v[32:47]
	v_max3_f32 v214, v214, v98, v83
	v_max3_f32 v214, v214, v99, v84
	s_waitcnt lgkmcnt(5)
	v_mfma_f32_32x32x16_bf16 v[48:63], v[120:123], v[148:151], v[48:63]
	v_max3_f32 v214, v214, v100, v85
	v_max3_f32 v214, v214, v101, v86
	s_waitcnt lgkmcnt(4)
	v_mfma_f32_32x32x16_bf16 v[64:79], v[124:127], v[148:151], v[64:79]
	v_max3_f32 v214, v214, v102, v87
	v_max3_f32 v214, v214, v103, v88
	s_waitcnt lgkmcnt(3)
	v_mfma_f32_32x32x16_bf16 v[48:63], v[128:131], v[152:155], v[48:63]
	v_max3_f32 v214, v214, v104, v89
	v_max3_f32 v214, v214, v105, v90
	s_waitcnt lgkmcnt(2)
	v_mfma_f32_32x32x16_bf16 v[64:79], v[132:135], v[152:155], v[64:79]
	v_max3_f32 v214, v214, v106, v91
	v_max3_f32 v214, v214, v107, v92
	s_waitcnt lgkmcnt(1)
	v_mfma_f32_32x32x16_bf16 v[48:63], v[136:139], v[156:159], v[48:63]
	v_max3_f32 v214, v214, v108, v93
	v_max3_f32 v214, v214, v109, v94
	s_waitcnt lgkmcnt(0)
	v_mfma_f32_32x32x16_bf16 v[64:79], v[140:143], v[156:159], v[64:79]
	v_max3_f32 v214, v214, v110, v95
	v_max_f32_e32 v214, v214, v111
	ds_bpermute_b32 v218, v227, v214
	v_add_u32_e32 v140, v211, v200
	v_add_u32_e32 v141, 31488, v140
	v_add_u32_e32 v140, 27136, v140
	ds_read2_b64 v[112:115], v140 offset1:2
	ds_read2_b64 v[116:119], v141 offset1:2
	ds_read2_b64 v[120:123], v140 offset0:4 offset1:6
	ds_read2_b64 v[124:127], v141 offset0:4 offset1:6
	ds_read2_b64 v[128:131], v140 offset0:8 offset1:10
	ds_read2_b64 v[132:135], v141 offset0:8 offset1:10
	ds_read2_b64 v[136:139], v140 offset0:12 offset1:14
	ds_read2_b64 v[140:143], v141 offset0:12 offset1:14
	s_waitcnt lgkmcnt(8)
	v_max_f32_e32 v214, v214, v218
	s_cmp_lg_u32 s40, 0
	s_cbranch_scc1 .Lfa_resc1
	v_cmp_lt_f32_e32 vcc, 0x40c00000, v214
	s_cbranch_vccnz .Lfa_resc1
.Lfa_cont1:
	v_exp_f32_e32 v80, v80
	v_exp_f32_e32 v81, v81
	v_exp_f32_e32 v82, v82
	v_exp_f32_e32 v83, v83
	v_exp_f32_e32 v84, v84
	v_exp_f32_e32 v85, v85
	v_exp_f32_e32 v86, v86
	v_exp_f32_e32 v87, v87
	v_add_f32_e32 v216, v80, v81
	v_add_f32_e32 v216, v216, v82
	v_add_f32_e32 v216, v216, v83
	v_add_f32_e32 v216, v216, v84
	v_add_f32_e32 v216, v216, v85
	v_add_f32_e32 v216, v216, v86
	v_add_f32_e32 v216, v216, v87
	v_cvt_pk_bf16_f32 v80, v80, v81
	v_cvt_pk_bf16_f32 v81, v82, v83
	v_cvt_pk_bf16_f32 v82, v84, v85
	v_cvt_pk_bf16_f32 v83, v86, v87
	v_exp_f32_e32 v88, v88
	v_exp_f32_e32 v89, v89
	v_exp_f32_e32 v90, v90
	v_exp_f32_e32 v91, v91
	s_waitcnt lgkmcnt(7)
	v_mfma_f32_32x32x16_bf16 v[0:15], v[112:115], v[80:83], v[0:15]
	v_exp_f32_e32 v92, v92
	v_exp_f32_e32 v93, v93
	v_exp_f32_e32 v94, v94
	v_exp_f32_e32 v95, v95
	s_waitcnt lgkmcnt(6)
	v_mfma_f32_32x32x16_bf16 v[16:31], v[116:119], v[80:83], v[16:31]
	v_add_f32_e32 v216, v216, v88
	v_add_f32_e32 v216, v216, v89
	v_add_f32_e32 v216, v216, v90
	v_add_f32_e32 v216, v216, v91
	v_add_f32_e32 v216, v216, v92
	v_add_f32_e32 v216, v216, v93
	v_add_f32_e32 v216, v216, v94
	v_add_f32_e32 v216, v216, v95
	v_cvt_pk_bf16_f32 v88, v88, v89
	v_cvt_pk_bf16_f32 v89, v90, v91
	v_cvt_pk_bf16_f32 v90, v92, v93
	v_cvt_pk_bf16_f32 v91, v94, v95
	v_exp_f32_e32 v96, v96
	v_exp_f32_e32 v97, v97
	v_exp_f32_e32 v98, v98
	v_exp_f32_e32 v99, v99
	s_waitcnt lgkmcnt(5)
	v_mfma_f32_32x32x16_bf16 v[0:15], v[120:123], v[88:91], v[0:15]
	v_exp_f32_e32 v100, v100
	v_exp_f32_e32 v101, v101
	v_exp_f32_e32 v102, v102
	v_exp_f32_e32 v103, v103
	s_waitcnt lgkmcnt(4)
	v_mfma_f32_32x32x16_bf16 v[16:31], v[124:127], v[88:91], v[16:31]
	v_add_f32_e32 v216, v216, v96
	v_add_f32_e32 v216, v216, v97
	v_add_f32_e32 v216, v216, v98
	v_add_f32_e32 v216, v216, v99
	v_add_f32_e32 v216, v216, v100
	v_add_f32_e32 v216, v216, v101
	v_add_f32_e32 v216, v216, v102
	v_add_f32_e32 v216, v216, v103
	v_cvt_pk_bf16_f32 v96, v96, v97
	v_cvt_pk_bf16_f32 v97, v98, v99
	v_cvt_pk_bf16_f32 v98, v100, v101
	v_cvt_pk_bf16_f32 v99, v102, v103
	v_exp_f32_e32 v104, v104
	v_exp_f32_e32 v105, v105
	v_exp_f32_e32 v106, v106
	v_exp_f32_e32 v107, v107
	s_waitcnt lgkmcnt(3)
	v_mfma_f32_32x32x16_bf16 v[0:15], v[128:131], v[96:99], v[0:15]
	v_exp_f32_e32 v108, v108
	v_exp_f32_e32 v109, v109
	v_exp_f32_e32 v110, v110
	v_exp_f32_e32 v111, v111
	s_waitcnt lgkmcnt(2)
	v_mfma_f32_32x32x16_bf16 v[16:31], v[132:135], v[96:99], v[16:31]
	v_add_f32_e32 v216, v216, v104
	v_add_f32_e32 v216, v216, v105
	v_add_f32_e32 v216, v216, v106
	v_add_f32_e32 v216, v216, v107
	v_add_f32_e32 v216, v216, v108
	v_add_f32_e32 v216, v216, v109
	v_add_f32_e32 v216, v216, v110
	v_add_f32_e32 v216, v216, v111
	v_cvt_pk_bf16_f32 v104, v104, v105
	v_cvt_pk_bf16_f32 v105, v106, v107
	v_cvt_pk_bf16_f32 v106, v108, v109
	v_cvt_pk_bf16_f32 v107, v110, v111
	v_add_f32_e32 v212, v212, v216
	s_waitcnt lgkmcnt(1)
	v_mfma_f32_32x32x16_bf16 v[0:15], v[136:139], v[104:107], v[0:15]
	s_waitcnt lgkmcnt(0)
	v_mfma_f32_32x32x16_bf16 v[16:31], v[140:143], v[104:107], v[16:31]
	s_barrier
	s_add_i32 s10, s29, 8
	s_min_i32 s10, s10, 0x43
	s_cmp_lt_i32 s10, 64
	s_cselect_b32 s11, s20, s41
	s_lshl_b32 s10, s10, 6
	s_add_i32 s10, s10, s11
	v_add_u32_e32 v112, s10, v197
	s_movk_i32 s10, 0x4a00
	v_mad_i64_i32 v[112:113], s[10:11], v112, s10, v[204:205]
	s_add_i32 s14, s29, 7
	s_min_i32 s14, s14, 0x43
	s_lshl_b32 s14, s14, 6
	s_mov_b32 s15, 0
	s_waitcnt vmcnt(7)
	ds_write_b128 v199, v[176:179]
	s_waitcnt vmcnt(6)
	ds_write2_b64 v217, v[180:181], v[182:183] offset1:1
	v_lshl_add_u64 v[114:115], s[14:15], 1, v[206:207]
	v_add_u32_e32 v216, v210, v208
	global_load_dwordx4 v[176:179], v[112:113], off
	global_load_dwordx4 v[180:183], v[114:115], off
	ds_read_b128 v[112:115], v216 offset:17920
	ds_read_b128 v[116:119], v216 offset:22528
	ds_read_b128 v[120:123], v216 offset:17952
	ds_read_b128 v[124:127], v216 offset:22560
	ds_read_b128 v[128:131], v216 offset:17984
	ds_read_b128 v[132:135], v216 offset:22592
	ds_read_b128 v[136:139], v216 offset:18016
	ds_read_b128 v[140:143], v216 offset:22624
	s_waitcnt lgkmcnt(7)
	v_mfma_f32_32x32x16_bf16 v[80:95], v[112:115], v[144:147], v[32:47]
	v_max3_f32 v214, v48, v64, v49
	v_max3_f32 v214, v214, v65, v50
	s_waitcnt lgkmcnt(6)
	v_mfma_f32_32x32x16_bf16 v[96:111], v[116:119], v[144:147], v[32:47]
	v_max3_f32 v214, v214, v66, v51
	v_max3_f32 v214, v214, v67, v52
	s_waitcnt lgkmcnt(5)
	v_mfma_f32_32x32x16_bf16 v[80:95], v[120:123], v[148:151], v[80:95]
	v_max3_f32 v214, v214, v68, v53
	v_max3_f32 v214, v214, v69, v54
	s_waitcnt lgkmcnt(4)
	v_mfma_f32_32x32x16_bf16 v[96:111], v[124:127], v[148:151], v[96:111]
	v_max3_f32 v214, v214, v70, v55
	v_max3_f32 v214, v214, v71, v56
	s_waitcnt lgkmcnt(3)
	v_mfma_f32_32x32x16_bf16 v[80:95], v[128:131], v[152:155], v[80:95]
	v_max3_f32 v214, v214, v72, v57
	v_max3_f32 v214, v214, v73, v58
	s_waitcnt lgkmcnt(2)
	v_mfma_f32_32x32x16_bf16 v[96:111], v[132:135], v[152:155], v[96:111]
	v_max3_f32 v214, v214, v74, v59
	v_max3_f32 v214, v214, v75, v60
	s_waitcnt lgkmcnt(1)
	v_mfma_f32_32x32x16_bf16 v[80:95], v[136:139], v[156:159], v[80:95]
	v_max3_f32 v214, v214, v76, v61
	v_max3_f32 v214, v214, v77, v62
	s_waitcnt lgkmcnt(0)
	v_mfma_f32_32x32x16_bf16 v[96:111], v[140:143], v[156:159], v[96:111]
	v_max3_f32 v214, v214, v78, v63
	v_max_f32_e32 v214, v214, v79
	ds_bpermute_b32 v218, v227, v214
	v_add_u32_e32 v140, v211, v200
	v_add_u32_e32 v141, 13568, v140
	v_add_u32_e32 v140, 9216, v140
	ds_read2_b64 v[112:115], v140 offset1:2
	ds_read2_b64 v[116:119], v141 offset1:2
	ds_read2_b64 v[120:123], v140 offset0:4 offset1:6
	ds_read2_b64 v[124:127], v141 offset0:4 offset1:6
	ds_read2_b64 v[128:131], v140 offset0:8 offset1:10
	ds_read2_b64 v[132:135], v141 offset0:8 offset1:10
	ds_read2_b64 v[136:139], v140 offset0:12 offset1:14
	ds_read2_b64 v[140:143], v141 offset0:12 offset1:14
	s_waitcnt lgkmcnt(8)
	v_max_f32_e32 v214, v214, v218
	s_cmp_lg_u32 s40, 0
	s_cbranch_scc1 .Lfa_resc2
	v_cmp_lt_f32_e32 vcc, 0x40c00000, v214
	s_cbranch_vccnz .Lfa_resc2
.Lfa_cont2:
	v_exp_f32_e32 v48, v48
	v_exp_f32_e32 v49, v49
	v_exp_f32_e32 v50, v50
	v_exp_f32_e32 v51, v51
	v_exp_f32_e32 v52, v52
	v_exp_f32_e32 v53, v53
	v_exp_f32_e32 v54, v54
	v_exp_f32_e32 v55, v55
	v_add_f32_e32 v216, v48, v49
	v_add_f32_e32 v216, v216, v50
	v_add_f32_e32 v216, v216, v51
	v_add_f32_e32 v216, v216, v52
	v_add_f32_e32 v216, v216, v53
	v_add_f32_e32 v216, v216, v54
	v_add_f32_e32 v216, v216, v55
	v_cvt_pk_bf16_f32 v48, v48, v49
	v_cvt_pk_bf16_f32 v49, v50, v51
	v_cvt_pk_bf16_f32 v50, v52, v53
	v_cvt_pk_bf16_f32 v51, v54, v55
	v_exp_f32_e32 v56, v56
	v_exp_f32_e32 v57, v57
	v_exp_f32_e32 v58, v58
	v_exp_f32_e32 v59, v59
	s_waitcnt lgkmcnt(7)
	v_mfma_f32_32x32x16_bf16 v[0:15], v[112:115], v[48:51], v[0:15]
	v_exp_f32_e32 v60, v60
	v_exp_f32_e32 v61, v61
	v_exp_f32_e32 v62, v62
	v_exp_f32_e32 v63, v63
	s_waitcnt lgkmcnt(6)
	v_mfma_f32_32x32x16_bf16 v[16:31], v[116:119], v[48:51], v[16:31]
	v_add_f32_e32 v216, v216, v56
	v_add_f32_e32 v216, v216, v57
	v_add_f32_e32 v216, v216, v58
	v_add_f32_e32 v216, v216, v59
	v_add_f32_e32 v216, v216, v60
	v_add_f32_e32 v216, v216, v61
	v_add_f32_e32 v216, v216, v62
	v_add_f32_e32 v216, v216, v63
	v_cvt_pk_bf16_f32 v56, v56, v57
	v_cvt_pk_bf16_f32 v57, v58, v59
	v_cvt_pk_bf16_f32 v58, v60, v61
	v_cvt_pk_bf16_f32 v59, v62, v63
	v_exp_f32_e32 v64, v64
	v_exp_f32_e32 v65, v65
	v_exp_f32_e32 v66, v66
	v_exp_f32_e32 v67, v67
	s_waitcnt lgkmcnt(5)
	v_mfma_f32_32x32x16_bf16 v[0:15], v[120:123], v[56:59], v[0:15]
	v_exp_f32_e32 v68, v68
	v_exp_f32_e32 v69, v69
	v_exp_f32_e32 v70, v70
	v_exp_f32_e32 v71, v71
	s_waitcnt lgkmcnt(4)
	v_mfma_f32_32x32x16_bf16 v[16:31], v[124:127], v[56:59], v[16:31]
	v_add_f32_e32 v216, v216, v64
	v_add_f32_e32 v216, v216, v65
	v_add_f32_e32 v216, v216, v66
	v_add_f32_e32 v216, v216, v67
	v_add_f32_e32 v216, v216, v68
	v_add_f32_e32 v216, v216, v69
	v_add_f32_e32 v216, v216, v70
	v_add_f32_e32 v216, v216, v71
	v_cvt_pk_bf16_f32 v64, v64, v65
	v_cvt_pk_bf16_f32 v65, v66, v67
	v_cvt_pk_bf16_f32 v66, v68, v69
	v_cvt_pk_bf16_f32 v67, v70, v71
	v_exp_f32_e32 v72, v72
	v_exp_f32_e32 v73, v73
	v_exp_f32_e32 v74, v74
	v_exp_f32_e32 v75, v75
	s_waitcnt lgkmcnt(3)
	v_mfma_f32_32x32x16_bf16 v[0:15], v[128:131], v[64:67], v[0:15]
	v_exp_f32_e32 v76, v76
	v_exp_f32_e32 v77, v77
	v_exp_f32_e32 v78, v78
	v_exp_f32_e32 v79, v79
	s_waitcnt lgkmcnt(2)
	v_mfma_f32_32x32x16_bf16 v[16:31], v[132:135], v[64:67], v[16:31]
	v_add_f32_e32 v216, v216, v72
	v_add_f32_e32 v216, v216, v73
	v_add_f32_e32 v216, v216, v74
	v_add_f32_e32 v216, v216, v75
	v_add_f32_e32 v216, v216, v76
	v_add_f32_e32 v216, v216, v77
	v_add_f32_e32 v216, v216, v78
	v_add_f32_e32 v216, v216, v79
	v_cvt_pk_bf16_f32 v72, v72, v73
	v_cvt_pk_bf16_f32 v73, v74, v75
	v_cvt_pk_bf16_f32 v74, v76, v77
	v_cvt_pk_bf16_f32 v75, v78, v79
	v_add_f32_e32 v212, v212, v216
	s_waitcnt lgkmcnt(1)
	v_mfma_f32_32x32x16_bf16 v[0:15], v[136:139], v[72:75], v[0:15]
	s_waitcnt lgkmcnt(0)
	v_mfma_f32_32x32x16_bf16 v[16:31], v[140:143], v[72:75], v[16:31]
	s_barrier
	s_add_i32 s10, s29, 9
	s_min_i32 s10, s10, 0x43
	s_cmp_lt_i32 s10, 64
	s_cselect_b32 s11, s20, s41
	s_lshl_b32 s10, s10, 6
	s_add_i32 s10, s10, s11
	v_add_u32_e32 v112, s10, v197
	s_movk_i32 s10, 0x4a00
	v_mad_i64_i32 v[112:113], s[10:11], v112, s10, v[204:205]
	s_add_i32 s14, s29, 8
	s_min_i32 s14, s14, 0x43
	s_lshl_b32 s14, s14, 6
	s_mov_b32 s15, 0
	s_waitcnt vmcnt(7)
	ds_write_b128 v199, v[184:187] offset:17920
	s_waitcnt vmcnt(6)
	ds_write2_b64 v203, v[188:189], v[190:191] offset1:1
	v_lshl_add_u64 v[114:115], s[14:15], 1, v[206:207]
	v_add_u32_e32 v216, v210, v208
	global_load_dwordx4 v[184:187], v[112:113], off
	global_load_dwordx4 v[188:191], v[114:115], off
	ds_read_b128 v[112:115], v216
	ds_read_b128 v[116:119], v216 offset:4608
	ds_read_b128 v[120:123], v216 offset:32
	ds_read_b128 v[124:127], v216 offset:4640
	ds_read_b128 v[128:131], v216 offset:64
	ds_read_b128 v[132:135], v216 offset:4672
	ds_read_b128 v[136:139], v216 offset:96
	ds_read_b128 v[140:143], v216 offset:4704
	s_waitcnt lgkmcnt(7)
	v_mfma_f32_32x32x16_bf16 v[48:63], v[112:115], v[144:147], v[32:47]
	v_max3_f32 v214, v80, v96, v81
	v_max3_f32 v214, v214, v97, v82
	s_waitcnt lgkmcnt(6)
	v_mfma_f32_32x32x16_bf16 v[64:79], v[116:119], v[144:147], v[32:47]
	v_max3_f32 v214, v214, v98, v83
	v_max3_f32 v214, v214, v99, v84
	s_waitcnt lgkmcnt(5)
	v_mfma_f32_32x32x16_bf16 v[48:63], v[120:123], v[148:151], v[48:63]
	v_max3_f32 v214, v214, v100, v85
	v_max3_f32 v214, v214, v101, v86
	s_waitcnt lgkmcnt(4)
	v_mfma_f32_32x32x16_bf16 v[64:79], v[124:127], v[148:151], v[64:79]
	v_max3_f32 v214, v214, v102, v87
	v_max3_f32 v214, v214, v103, v88
	s_waitcnt lgkmcnt(3)
	v_mfma_f32_32x32x16_bf16 v[48:63], v[128:131], v[152:155], v[48:63]
	v_max3_f32 v214, v214, v104, v89
	v_max3_f32 v214, v214, v105, v90
	s_waitcnt lgkmcnt(2)
	v_mfma_f32_32x32x16_bf16 v[64:79], v[132:135], v[152:155], v[64:79]
	v_max3_f32 v214, v214, v106, v91
	v_max3_f32 v214, v214, v107, v92
	s_waitcnt lgkmcnt(1)
	v_mfma_f32_32x32x16_bf16 v[48:63], v[136:139], v[156:159], v[48:63]
	v_max3_f32 v214, v214, v108, v93
	v_max3_f32 v214, v214, v109, v94
	s_waitcnt lgkmcnt(0)
	v_mfma_f32_32x32x16_bf16 v[64:79], v[140:143], v[156:159], v[64:79]
	v_max3_f32 v214, v214, v110, v95
	v_max_f32_e32 v214, v214, v111
	ds_bpermute_b32 v218, v227, v214
	v_add_u32_e32 v140, v211, v200
	v_add_u32_e32 v141, 31488, v140
	v_add_u32_e32 v140, 27136, v140
	ds_read2_b64 v[112:115], v140 offset1:2
	ds_read2_b64 v[116:119], v141 offset1:2
	ds_read2_b64 v[120:123], v140 offset0:4 offset1:6
	ds_read2_b64 v[124:127], v141 offset0:4 offset1:6
	ds_read2_b64 v[128:131], v140 offset0:8 offset1:10
	ds_read2_b64 v[132:135], v141 offset0:8 offset1:10
	ds_read2_b64 v[136:139], v140 offset0:12 offset1:14
	ds_read2_b64 v[140:143], v141 offset0:12 offset1:14
	s_waitcnt lgkmcnt(8)
	v_max_f32_e32 v214, v214, v218
	s_cmp_lg_u32 s40, 0
	s_cbranch_scc1 .Lfa_resc3
	v_cmp_lt_f32_e32 vcc, 0x40c00000, v214
	s_cbranch_vccnz .Lfa_resc3
.Lfa_cont3:
	v_exp_f32_e32 v80, v80
	v_exp_f32_e32 v81, v81
	v_exp_f32_e32 v82, v82
	v_exp_f32_e32 v83, v83
	v_exp_f32_e32 v84, v84
	v_exp_f32_e32 v85, v85
	v_exp_f32_e32 v86, v86
	v_exp_f32_e32 v87, v87
	v_add_f32_e32 v216, v80, v81
	v_add_f32_e32 v216, v216, v82
	v_add_f32_e32 v216, v216, v83
	v_add_f32_e32 v216, v216, v84
	v_add_f32_e32 v216, v216, v85
	v_add_f32_e32 v216, v216, v86
	v_add_f32_e32 v216, v216, v87
	v_cvt_pk_bf16_f32 v80, v80, v81
	v_cvt_pk_bf16_f32 v81, v82, v83
	v_cvt_pk_bf16_f32 v82, v84, v85
	v_cvt_pk_bf16_f32 v83, v86, v87
	v_exp_f32_e32 v88, v88
	v_exp_f32_e32 v89, v89
	v_exp_f32_e32 v90, v90
	v_exp_f32_e32 v91, v91
	s_waitcnt lgkmcnt(7)
	v_mfma_f32_32x32x16_bf16 v[0:15], v[112:115], v[80:83], v[0:15]
	v_exp_f32_e32 v92, v92
	v_exp_f32_e32 v93, v93
	v_exp_f32_e32 v94, v94
	v_exp_f32_e32 v95, v95
	s_waitcnt lgkmcnt(6)
	v_mfma_f32_32x32x16_bf16 v[16:31], v[116:119], v[80:83], v[16:31]
	v_add_f32_e32 v216, v216, v88
	v_add_f32_e32 v216, v216, v89
	v_add_f32_e32 v216, v216, v90
	v_add_f32_e32 v216, v216, v91
	v_add_f32_e32 v216, v216, v92
	v_add_f32_e32 v216, v216, v93
	v_add_f32_e32 v216, v216, v94
	v_add_f32_e32 v216, v216, v95
	v_cvt_pk_bf16_f32 v88, v88, v89
	v_cvt_pk_bf16_f32 v89, v90, v91
	v_cvt_pk_bf16_f32 v90, v92, v93
	v_cvt_pk_bf16_f32 v91, v94, v95
	v_exp_f32_e32 v96, v96
	v_exp_f32_e32 v97, v97
	v_exp_f32_e32 v98, v98
	v_exp_f32_e32 v99, v99
	s_waitcnt lgkmcnt(5)
	v_mfma_f32_32x32x16_bf16 v[0:15], v[120:123], v[88:91], v[0:15]
	v_exp_f32_e32 v100, v100
	v_exp_f32_e32 v101, v101
	v_exp_f32_e32 v102, v102
	v_exp_f32_e32 v103, v103
	s_waitcnt lgkmcnt(4)
	v_mfma_f32_32x32x16_bf16 v[16:31], v[124:127], v[88:91], v[16:31]
	v_add_f32_e32 v216, v216, v96
	v_add_f32_e32 v216, v216, v97
	v_add_f32_e32 v216, v216, v98
	v_add_f32_e32 v216, v216, v99
	v_add_f32_e32 v216, v216, v100
	v_add_f32_e32 v216, v216, v101
	v_add_f32_e32 v216, v216, v102
	v_add_f32_e32 v216, v216, v103
	v_cvt_pk_bf16_f32 v96, v96, v97
	v_cvt_pk_bf16_f32 v97, v98, v99
	v_cvt_pk_bf16_f32 v98, v100, v101
	v_cvt_pk_bf16_f32 v99, v102, v103
	v_exp_f32_e32 v104, v104
	v_exp_f32_e32 v105, v105
	v_exp_f32_e32 v106, v106
	v_exp_f32_e32 v107, v107
	s_waitcnt lgkmcnt(3)
	v_mfma_f32_32x32x16_bf16 v[0:15], v[128:131], v[96:99], v[0:15]
	v_exp_f32_e32 v108, v108
	v_exp_f32_e32 v109, v109
	v_exp_f32_e32 v110, v110
	v_exp_f32_e32 v111, v111
	s_waitcnt lgkmcnt(2)
	v_mfma_f32_32x32x16_bf16 v[16:31], v[132:135], v[96:99], v[16:31]
	v_add_f32_e32 v216, v216, v104
	v_add_f32_e32 v216, v216, v105
	v_add_f32_e32 v216, v216, v106
	v_add_f32_e32 v216, v216, v107
	v_add_f32_e32 v216, v216, v108
	v_add_f32_e32 v216, v216, v109
	v_add_f32_e32 v216, v216, v110
	v_add_f32_e32 v216, v216, v111
	v_cvt_pk_bf16_f32 v104, v104, v105
	v_cvt_pk_bf16_f32 v105, v106, v107
	v_cvt_pk_bf16_f32 v106, v108, v109
	v_cvt_pk_bf16_f32 v107, v110, v111
	v_add_f32_e32 v212, v212, v216
	s_waitcnt lgkmcnt(1)
	v_mfma_f32_32x32x16_bf16 v[0:15], v[136:139], v[104:107], v[0:15]
	s_waitcnt lgkmcnt(0)
	v_mfma_f32_32x32x16_bf16 v[16:31], v[140:143], v[104:107], v[16:31]
	s_barrier
	s_add_i32 s29, s29, 4
	s_cmp_lt_i32 s29, 68
	s_cbranch_scc1 .Lfa_loop
	s_branch .LBB0_908
.Lfa_resc0:
	s_nop 7
	s_nop 7
	s_cmp_lg_u32 s40, 0
	s_cselect_b32 s10, 0xc2f00000, 0
	v_max_f32_e32 v214, s10, v214
	v_exp_f32_e64 v218, -v214
	v_add_f32_e32 v215, v215, v214
	v_xor_b32_e32 v32, 0x80000000, v215
	v_mul_f32_e32 v212, v212, v218
	v_mul_f32_e32 v0, v0, v218
	v_mul_f32_e32 v1, v1, v218
	v_mul_f32_e32 v2, v2, v218
	v_mul_f32_e32 v3, v3, v218
	v_mul_f32_e32 v4, v4, v218
	v_mul_f32_e32 v5, v5, v218
	v_mul_f32_e32 v6, v6, v218
	v_mul_f32_e32 v7, v7, v218
	v_mul_f32_e32 v8, v8, v218
	v_mul_f32_e32 v9, v9, v218
	v_mul_f32_e32 v10, v10, v218
	v_mul_f32_e32 v11, v11, v218
	v_mul_f32_e32 v12, v12, v218
	v_mul_f32_e32 v13, v13, v218
	v_mul_f32_e32 v14, v14, v218
	v_mul_f32_e32 v15, v15, v218
	v_mul_f32_e32 v16, v16, v218
	v_mul_f32_e32 v17, v17, v218
	v_mul_f32_e32 v18, v18, v218
	v_mul_f32_e32 v19, v19, v218
	v_mul_f32_e32 v20, v20, v218
	v_mul_f32_e32 v21, v21, v218
	v_mul_f32_e32 v22, v22, v218
	v_mul_f32_e32 v23, v23, v218
	v_mul_f32_e32 v24, v24, v218
	v_mul_f32_e32 v25, v25, v218
	v_mul_f32_e32 v26, v26, v218
	v_mul_f32_e32 v27, v27, v218
	v_mul_f32_e32 v28, v28, v218
	v_mul_f32_e32 v29, v29, v218
	v_mul_f32_e32 v30, v30, v218
	v_mul_f32_e32 v31, v31, v218
	v_sub_f32_e32 v48, v48, v214
	v_sub_f32_e32 v49, v49, v214
	v_sub_f32_e32 v50, v50, v214
	v_sub_f32_e32 v51, v51, v214
	v_sub_f32_e32 v52, v52, v214
	v_sub_f32_e32 v53, v53, v214
	v_sub_f32_e32 v54, v54, v214
	v_sub_f32_e32 v55, v55, v214
	v_sub_f32_e32 v56, v56, v214
	v_sub_f32_e32 v57, v57, v214
	v_sub_f32_e32 v58, v58, v214
	v_sub_f32_e32 v59, v59, v214
	v_sub_f32_e32 v60, v60, v214
	v_sub_f32_e32 v61, v61, v214
	v_sub_f32_e32 v62, v62, v214
	v_sub_f32_e32 v63, v63, v214
	v_sub_f32_e32 v64, v64, v214
	v_sub_f32_e32 v65, v65, v214
	v_sub_f32_e32 v66, v66, v214
	v_sub_f32_e32 v67, v67, v214
	v_sub_f32_e32 v68, v68, v214
	v_sub_f32_e32 v69, v69, v214
	v_sub_f32_e32 v70, v70, v214
	v_sub_f32_e32 v71, v71, v214
	v_sub_f32_e32 v72, v72, v214
	v_sub_f32_e32 v73, v73, v214
	v_sub_f32_e32 v74, v74, v214
	v_sub_f32_e32 v75, v75, v214
	v_sub_f32_e32 v76, v76, v214
	v_sub_f32_e32 v77, v77, v214
	v_sub_f32_e32 v78, v78, v214
	v_sub_f32_e32 v79, v79, v214
	v_sub_f32_e32 v80, v80, v214
	v_sub_f32_e32 v81, v81, v214
	v_sub_f32_e32 v82, v82, v214
	v_sub_f32_e32 v83, v83, v214
	v_sub_f32_e32 v84, v84, v214
	v_sub_f32_e32 v85, v85, v214
	v_sub_f32_e32 v86, v86, v214
	v_sub_f32_e32 v87, v87, v214
	v_sub_f32_e32 v88, v88, v214
	v_sub_f32_e32 v89, v89, v214
	v_sub_f32_e32 v90, v90, v214
	v_sub_f32_e32 v91, v91, v214
	v_sub_f32_e32 v92, v92, v214
	v_sub_f32_e32 v93, v93, v214
	v_sub_f32_e32 v94, v94, v214
	v_sub_f32_e32 v95, v95, v214
	v_sub_f32_e32 v96, v96, v214
	v_sub_f32_e32 v97, v97, v214
	v_sub_f32_e32 v98, v98, v214
	v_sub_f32_e32 v99, v99, v214
	v_sub_f32_e32 v100, v100, v214
	v_sub_f32_e32 v101, v101, v214
	v_sub_f32_e32 v102, v102, v214
	v_sub_f32_e32 v103, v103, v214
	v_sub_f32_e32 v104, v104, v214
	v_sub_f32_e32 v105, v105, v214
	v_sub_f32_e32 v106, v106, v214
	v_sub_f32_e32 v107, v107, v214
	v_sub_f32_e32 v108, v108, v214
	v_sub_f32_e32 v109, v109, v214
	v_sub_f32_e32 v110, v110, v214
	v_sub_f32_e32 v111, v111, v214
	v_mov_b32_e32 v33, v32
	v_mov_b32_e32 v34, v32
	v_mov_b32_e32 v35, v32
	v_mov_b32_e32 v36, v32
	v_mov_b32_e32 v37, v32
	v_mov_b32_e32 v38, v32
	v_mov_b32_e32 v39, v32
	v_mov_b32_e32 v40, v32
	v_mov_b32_e32 v41, v32
	v_mov_b32_e32 v42, v32
	v_mov_b32_e32 v43, v32
	v_mov_b32_e32 v44, v32
	v_mov_b32_e32 v45, v32
	v_mov_b32_e32 v46, v32
	v_mov_b32_e32 v47, v32
	s_mov_b32 s40, 0
	s_branch .Lfa_cont0
.Lfa_resc1:
	s_nop 7
	s_nop 7
	s_cmp_lg_u32 s40, 0
	s_cselect_b32 s10, 0xc2f00000, 0
	v_max_f32_e32 v214, s10, v214
	v_exp_f32_e64 v218, -v214
	v_add_f32_e32 v215, v215, v214
	v_xor_b32_e32 v32, 0x80000000, v215
	v_mul_f32_e32 v212, v212, v218
	v_mul_f32_e32 v0, v0, v218
	v_mul_f32_e32 v1, v1, v218
	v_mul_f32_e32 v2, v2, v218
	v_mul_f32_e32 v3, v3, v218
	v_mul_f32_e32 v4, v4, v218
	v_mul_f32_e32 v5, v5, v218
	v_mul_f32_e32 v6, v6, v218
	v_mul_f32_e32 v7, v7, v218
	v_mul_f32_e32 v8, v8, v218
	v_mul_f32_e32 v9, v9, v218
	v_mul_f32_e32 v10, v10, v218
	v_mul_f32_e32 v11, v11, v218
	v_mul_f32_e32 v12, v12, v218
	v_mul_f32_e32 v13, v13, v218
	v_mul_f32_e32 v14, v14, v218
	v_mul_f32_e32 v15, v15, v218
	v_mul_f32_e32 v16, v16, v218
	v_mul_f32_e32 v17, v17, v218
	v_mul_f32_e32 v18, v18, v218
	v_mul_f32_e32 v19, v19, v218
	v_mul_f32_e32 v20, v20, v218
	v_mul_f32_e32 v21, v21, v218
	v_mul_f32_e32 v22, v22, v218
	v_mul_f32_e32 v23, v23, v218
	v_mul_f32_e32 v24, v24, v218
	v_mul_f32_e32 v25, v25, v218
	v_mul_f32_e32 v26, v26, v218
	v_mul_f32_e32 v27, v27, v218
	v_mul_f32_e32 v28, v28, v218
	v_mul_f32_e32 v29, v29, v218
	v_mul_f32_e32 v30, v30, v218
	v_mul_f32_e32 v31, v31, v218
	v_sub_f32_e32 v80, v80, v214
	v_sub_f32_e32 v81, v81, v214
	v_sub_f32_e32 v82, v82, v214
	v_sub_f32_e32 v83, v83, v214
	v_sub_f32_e32 v84, v84, v214
	v_sub_f32_e32 v85, v85, v214
	v_sub_f32_e32 v86, v86, v214
	v_sub_f32_e32 v87, v87, v214
	v_sub_f32_e32 v88, v88, v214
	v_sub_f32_e32 v89, v89, v214
	v_sub_f32_e32 v90, v90, v214
	v_sub_f32_e32 v91, v91, v214
	v_sub_f32_e32 v92, v92, v214
	v_sub_f32_e32 v93, v93, v214
	v_sub_f32_e32 v94, v94, v214
	v_sub_f32_e32 v95, v95, v214
	v_sub_f32_e32 v96, v96, v214
	v_sub_f32_e32 v97, v97, v214
	v_sub_f32_e32 v98, v98, v214
	v_sub_f32_e32 v99, v99, v214
	v_sub_f32_e32 v100, v100, v214
	v_sub_f32_e32 v101, v101, v214
	v_sub_f32_e32 v102, v102, v214
	v_sub_f32_e32 v103, v103, v214
	v_sub_f32_e32 v104, v104, v214
	v_sub_f32_e32 v105, v105, v214
	v_sub_f32_e32 v106, v106, v214
	v_sub_f32_e32 v107, v107, v214
	v_sub_f32_e32 v108, v108, v214
	v_sub_f32_e32 v109, v109, v214
	v_sub_f32_e32 v110, v110, v214
	v_sub_f32_e32 v111, v111, v214
	v_sub_f32_e32 v48, v48, v214
	v_sub_f32_e32 v49, v49, v214
	v_sub_f32_e32 v50, v50, v214
	v_sub_f32_e32 v51, v51, v214
	v_sub_f32_e32 v52, v52, v214
	v_sub_f32_e32 v53, v53, v214
	v_sub_f32_e32 v54, v54, v214
	v_sub_f32_e32 v55, v55, v214
	v_sub_f32_e32 v56, v56, v214
	v_sub_f32_e32 v57, v57, v214
	v_sub_f32_e32 v58, v58, v214
	v_sub_f32_e32 v59, v59, v214
	v_sub_f32_e32 v60, v60, v214
	v_sub_f32_e32 v61, v61, v214
	v_sub_f32_e32 v62, v62, v214
	v_sub_f32_e32 v63, v63, v214
	v_sub_f32_e32 v64, v64, v214
	v_sub_f32_e32 v65, v65, v214
	v_sub_f32_e32 v66, v66, v214
	v_sub_f32_e32 v67, v67, v214
	v_sub_f32_e32 v68, v68, v214
	v_sub_f32_e32 v69, v69, v214
	v_sub_f32_e32 v70, v70, v214
	v_sub_f32_e32 v71, v71, v214
	v_sub_f32_e32 v72, v72, v214
	v_sub_f32_e32 v73, v73, v214
	v_sub_f32_e32 v74, v74, v214
	v_sub_f32_e32 v75, v75, v214
	v_sub_f32_e32 v76, v76, v214
	v_sub_f32_e32 v77, v77, v214
	v_sub_f32_e32 v78, v78, v214
	v_sub_f32_e32 v79, v79, v214
	v_mov_b32_e32 v33, v32
	v_mov_b32_e32 v34, v32
	v_mov_b32_e32 v35, v32
	v_mov_b32_e32 v36, v32
	v_mov_b32_e32 v37, v32
	v_mov_b32_e32 v38, v32
	v_mov_b32_e32 v39, v32
	v_mov_b32_e32 v40, v32
	v_mov_b32_e32 v41, v32
	v_mov_b32_e32 v42, v32
	v_mov_b32_e32 v43, v32
	v_mov_b32_e32 v44, v32
	v_mov_b32_e32 v45, v32
	v_mov_b32_e32 v46, v32
	v_mov_b32_e32 v47, v32
	s_mov_b32 s40, 0
	s_branch .Lfa_cont1
